# baseline (speedup 1.0000x reference)
.LBB1_34:
	s_add_i32 s51, s25, 3
	s_sub_i32 s51, s51, s50
	s_cmp_ge_i32 s51, 2
	s_cbranch_scc1 .Lsqk_0b
	s_cmp_ge_i32 s51, 1
	s_cbranch_scc1 .Lfqk_0b
	v_add_u32_e32 v206, s43, v209
	ds_read_b64_tr_b16 v[186:187], v206 offset:24576
	ds_read_b64_tr_b16 v[188:189], v206 offset:25088
	s_waitcnt lgkmcnt(9)
	v_mfma_f32_32x32x16_f16 v[66:81], v[174:177], v[142:145], v[34:49]
	v_add_f32_e32 v50, v98, v99
	v_add_f32_e32 v50, v100, v50
	v_add_f32_e32 v50, v101, v50
	v_add_f32_e32 v50, v102, v50
	v_add_f32_e32 v50, v103, v50
	v_cvt_pk_f16_f32 v134, v98, v99
	v_cvt_pk_f16_f32 v135, v100, v101
	ds_read_b64_tr_b16 v[182:183], v206 offset:28672
	ds_read_b64_tr_b16 v[184:185], v206 offset:29184
	v_add_f32_e32 v50, v104, v50
	v_add_f32_e32 v50, v105, v50
	v_add_f32_e32 v50, v106, v50
	v_add_f32_e32 v98, v107, v50
	s_waitcnt lgkmcnt(10)
	v_mfma_f32_32x32x16_f16 v[50:65], v[170:173], v[142:145], v[34:49]
	v_cvt_pk_f16_f32 v136, v102, v103
	v_cvt_pk_f16_f32 v137, v104, v105
	ds_read_b64_tr_b16 v[178:179], v206 offset:25600
	ds_read_b64_tr_b16 v[180:181], v206 offset:26112
	s_waitcnt lgkmcnt(11)
	v_mfma_f32_32x32x16_f16 v[66:81], v[166:169], v[138:141], v[66:81]
	v_add_f32_e32 v98, v108, v98
	v_add_f32_e32 v98, v109, v98
	v_add_f32_e32 v98, v110, v98
	v_add_f32_e32 v98, v111, v98
	v_cvt_pk_f16_f32 v126, v106, v107
	v_cvt_pk_f16_f32 v127, v108, v109
	ds_read_b64_tr_b16 v[106:107], v206 offset:29696
	ds_read_b64_tr_b16 v[108:109], v206 offset:30208
	s_waitcnt lgkmcnt(12)
	v_mfma_f32_32x32x16_f16 v[50:65], v[162:165], v[138:141], v[50:65]
	v_add_f32_e32 v98, v112, v98
	v_add_f32_e32 v98, v113, v98
	v_add_f32_e32 v98, v82, v98
	v_add_f32_e32 v98, v83, v98
	v_cvt_pk_f16_f32 v128, v110, v111
	v_cvt_pk_f16_f32 v129, v112, v113
	ds_read_b64_tr_b16 v[102:103], v206 offset:26624
	ds_read_b64_tr_b16 v[104:105], v206 offset:27136
	s_waitcnt lgkmcnt(13)
	v_mfma_f32_32x32x16_f16 v[66:81], v[158:161], v[130:133], v[66:81]
	v_add_f32_e32 v98, v84, v98
	v_add_f32_e32 v98, v85, v98
	v_add_f32_e32 v98, v86, v98
	v_add_f32_e32 v110, v87, v98
	v_cvt_pk_f16_f32 v118, v82, v83
	v_cvt_pk_f16_f32 v119, v84, v85
	ds_read_b64_tr_b16 v[98:99], v206 offset:30720
	ds_read_b64_tr_b16 v[100:101], v206 offset:31232
	s_waitcnt lgkmcnt(14)
	v_mfma_f32_32x32x16_f16 v[50:65], v[154:157], v[130:133], v[50:65]
	v_add_f32_e32 v82, v88, v110
	v_add_f32_e32 v82, v89, v82
	v_add_f32_e32 v82, v90, v82
	v_add_f32_e32 v82, v91, v82
	v_cvt_pk_f16_f32 v120, v86, v87
	v_cvt_pk_f16_f32 v121, v88, v89
	ds_read_b64_tr_b16 v[86:87], v206 offset:27648
	ds_read_b64_tr_b16 v[88:89], v206 offset:28160
	s_waitcnt lgkmcnt(14)
	v_mfma_f32_32x32x16_f16 v[66:81], v[150:153], v[122:125], v[66:81]
	v_add_f32_e32 v82, v92, v82
	v_add_f32_e32 v82, v93, v82
	v_add_f32_e32 v82, v94, v82
	v_add_f32_e32 v110, v95, v82
	v_cvt_pk_f16_f32 v114, v90, v91
	v_cvt_pk_f16_f32 v115, v92, v93
	ds_read_b64_tr_b16 v[82:83], v206 offset:31744
	ds_read_b64_tr_b16 v[84:85], v206 offset:32256
	v_mfma_f32_32x32x16_f16 v[50:65], v[146:149], v[122:125], v[50:65]
	v_add_f32_e32 v90, v96, v110
	v_add_f32_e32 v90, v97, v90
	v_add_f32_e32 v90, 0, v90
	v_cvt_pk_f16_f32 v116, v94, v95
	v_cvt_pk_f16_f32 v117, v96, v97
.Lsqk_0b:
	s_add_i32 s47, s24, 2
	s_cmp_ge_u32 s47, s41
	s_cselect_b64 s[22:23], -1, 0
	s_and_b64 vcc, exec, s[22:23]
	s_cbranch_vccnz .LBB1_36
	s_add_i32 s2, s44, s39
	s_mov_b32 s3, m0
	s_mov_b32 m0, s2
	s_nop 0
	global_load_lds_dwordx4 v211, s[16:17]
	s_mov_b32 m0, s3

.LBB1_38:
	s_add_i32 s25, s25, 3
	s_cmp_lt_i32 s25, s50
	s_cbranch_scc1 .LBB1_40
	s_sub_i32 s51, s25, s50
	s_cmp_ge_i32 s51, 2
	s_cbranch_scc1 .Lsall_0b
	s_cmp_gt_i32 s25, s50
	s_cbranch_scc1 .Lmfill_0b
	v_subrev_u32_e32 v92, 27, v201
	v_subrev_u32_e32 v91, 59, v201
	v_cmp_le_u32_e32 vcc, v92, v204
	s_nop 1
	v_cndmask_b32_e32 v50, v205, v50, vcc
	v_cmp_lt_u32_e32 vcc, v91, v204
	s_nop 1
	v_cndmask_b32_e32 v67, v205, v67, vcc
	v_cmp_le_u32_e32 vcc, v91, v204
	v_subrev_u32_e32 v91, 26, v201
	s_nop 0
	v_cndmask_b32_e32 v66, v205, v66, vcc
	v_cmp_le_u32_e32 vcc, v91, v204
	v_subrev_u32_e32 v91, 57, v201
	s_nop 0
	v_cndmask_b32_e32 v51, v205, v51, vcc
	v_cmp_le_u32_e32 vcc, v91, v204
	v_subrev_u32_e32 v91, 25, v201
	s_nop 0
	v_cndmask_b32_e32 v68, v205, v68, vcc
	v_cmp_le_u32_e32 vcc, v91, v204
	v_subrev_u32_e32 v91, 56, v201
	s_nop 0
	v_cndmask_b32_e32 v52, v205, v52, vcc
	v_cmp_le_u32_e32 vcc, v91, v204
	v_subrev_u32_e32 v91, 24, v201
	s_nop 0
	v_cndmask_b32_e32 v69, v205, v69, vcc
	v_cmp_le_u32_e32 vcc, v91, v204
	v_subrev_u32_e32 v91, 51, v201
	s_nop 0
	v_cndmask_b32_e32 v53, v205, v53, vcc
	v_cmp_le_u32_e32 vcc, v91, v204
	v_subrev_u32_e32 v91, 19, v201
	s_nop 0
	v_cndmask_b32_e32 v70, v205, v70, vcc
	v_cmp_le_u32_e32 vcc, v91, v204
	v_subrev_u32_e32 v91, 50, v201
	s_nop 0
	v_cndmask_b32_e32 v54, v205, v54, vcc
	v_cmp_le_u32_e32 vcc, v91, v204
	v_subrev_u32_e32 v91, 18, v201
	s_nop 0
	v_cndmask_b32_e32 v71, v205, v71, vcc
	v_cmp_le_u32_e32 vcc, v91, v204
	v_subrev_u32_e32 v91, 49, v201
	s_nop 0
	v_cndmask_b32_e32 v55, v205, v55, vcc
	v_cmp_le_u32_e32 vcc, v91, v204
	v_subrev_u32_e32 v91, 17, v201
	s_nop 0
	v_cndmask_b32_e32 v72, v205, v72, vcc
	v_cmp_le_u32_e32 vcc, v91, v204
	v_subrev_u32_e32 v91, 48, v201
	s_nop 0
	v_cndmask_b32_e32 v56, v205, v56, vcc
	v_cmp_le_u32_e32 vcc, v91, v204
	v_add_u32_e32 v91, -16, v201
	s_nop 0
	v_cndmask_b32_e32 v73, v205, v73, vcc
	v_cmp_le_u32_e32 vcc, v91, v204
	v_subrev_u32_e32 v91, 43, v201
	s_nop 0
	v_cndmask_b32_e32 v57, v205, v57, vcc
	v_cmp_le_u32_e32 vcc, v91, v204
	v_add_u32_e32 v91, -11, v201
	s_nop 0
	v_cndmask_b32_e32 v74, v205, v74, vcc
	v_cmp_le_u32_e32 vcc, v91, v204
	v_subrev_u32_e32 v91, 42, v201
	s_nop 0
	v_cndmask_b32_e32 v58, v205, v58, vcc
	v_cmp_le_u32_e32 vcc, v91, v204
	v_add_u32_e32 v91, -10, v201
	s_nop 0
	v_cndmask_b32_e32 v75, v205, v75, vcc
	v_cmp_le_u32_e32 vcc, v91, v204
	v_subrev_u32_e32 v91, 41, v201
	s_nop 0
	v_cndmask_b32_e32 v59, v205, v59, vcc
	v_cmp_le_u32_e32 vcc, v91, v204
	v_add_u32_e32 v91, -9, v201
	s_nop 0
	v_cndmask_b32_e32 v76, v205, v76, vcc
	v_cmp_le_u32_e32 vcc, v91, v204
	v_subrev_u32_e32 v91, 40, v201
	s_nop 0
	v_cndmask_b32_e32 v60, v205, v60, vcc
	v_cmp_le_u32_e32 vcc, v91, v204
	v_add_u32_e32 v91, -8, v201
	s_nop 0
	v_cndmask_b32_e32 v77, v205, v77, vcc
	v_cmp_le_u32_e32 vcc, v91, v204
	v_subrev_u32_e32 v91, 35, v201
	s_nop 0
	v_cndmask_b32_e32 v61, v205, v61, vcc
	v_cmp_le_u32_e32 vcc, v91, v204
	v_add_u32_e32 v91, -3, v201
	s_nop 0
	v_cndmask_b32_e32 v78, v205, v78, vcc
	v_cmp_le_u32_e32 vcc, v91, v204
	v_subrev_u32_e32 v91, 34, v201
	s_nop 0
	v_cndmask_b32_e32 v62, v205, v62, vcc
	v_cmp_le_u32_e32 vcc, v91, v204
	v_add_u32_e32 v91, -2, v201
	s_nop 0
	v_cndmask_b32_e32 v79, v205, v79, vcc
	v_cmp_le_u32_e32 vcc, v91, v204
	v_subrev_u32_e32 v91, 33, v201
	s_nop 0
	v_cndmask_b32_e32 v63, v205, v63, vcc
	v_cmp_le_u32_e32 vcc, v91, v204
	v_add_u32_e32 v91, -1, v201
	s_nop 0
	v_cndmask_b32_e32 v80, v205, v80, vcc
	v_cmp_le_u32_e32 vcc, v91, v204
	v_subrev_u32_e32 v91, 32, v201
	s_nop 0
	v_cndmask_b32_e32 v64, v205, v64, vcc
	v_cmp_le_u32_e32 vcc, v91, v204
	s_nop 1
	v_cndmask_b32_e32 v81, v205, v81, vcc
	v_cmp_le_u32_e32 vcc, v201, v204
	s_nop 1
	v_cndmask_b32_e32 v65, v205, v65, vcc

.LBB1_121:
	s_add_i32 s51, s14, 3
	s_sub_i32 s51, s51, s50
	s_cmp_ge_i32 s51, 2
	s_cbranch_scc1 .Lsqk_1b
	s_cmp_ge_i32 s51, 1
	s_cbranch_scc1 .Lfqk_1b
	v_add_u32_e32 v68, s25, v251
	ds_read_b64_tr_b16 v[200:201], v68
	ds_read_b64_tr_b16 v[202:203], v68 offset:512
	s_waitcnt lgkmcnt(9)
	v_mfma_f32_32x32x16_f16 v[80:95], v[188:191], v[140:143], v[32:47]
	v_add_f32_e32 v48, v112, v113
	v_add_f32_e32 v48, v114, v48
	v_add_f32_e32 v48, v115, v48
	v_add_f32_e32 v48, v116, v48
	v_add_f32_e32 v48, v117, v48
	v_cvt_pk_f16_f32 v156, v112, v113
	v_cvt_pk_f16_f32 v157, v114, v115
	ds_read_b64_tr_b16 v[196:197], v68 offset:4096
	ds_read_b64_tr_b16 v[198:199], v68 offset:4608
	v_add_f32_e32 v48, v118, v48
	v_add_f32_e32 v48, v119, v48
	v_add_f32_e32 v48, v120, v48
	v_add_f32_e32 v66, v121, v48
	s_waitcnt lgkmcnt(10)
	v_mfma_f32_32x32x16_f16 v[48:63], v[184:187], v[140:143], v[32:47]
	v_cvt_pk_f16_f32 v158, v116, v117
	v_cvt_pk_f16_f32 v159, v118, v119
	ds_read_b64_tr_b16 v[192:193], v68 offset:1024
	ds_read_b64_tr_b16 v[194:195], v68 offset:1536
	s_waitcnt lgkmcnt(11)
	v_mfma_f32_32x32x16_f16 v[80:95], v[180:183], v[136:139], v[80:95]
	v_add_f32_e32 v66, v122, v66
	v_add_f32_e32 v66, v123, v66
	v_add_f32_e32 v66, v124, v66
	v_add_f32_e32 v66, v125, v66
	v_cvt_pk_f16_f32 v152, v120, v121
	v_cvt_pk_f16_f32 v153, v122, v123
	ds_read_b64_tr_b16 v[116:117], v68 offset:5120
	ds_read_b64_tr_b16 v[118:119], v68 offset:5632
	s_waitcnt lgkmcnt(12)
	v_mfma_f32_32x32x16_f16 v[48:63], v[176:179], v[136:139], v[48:63]
	v_add_f32_e32 v66, v126, v66
	v_add_f32_e32 v66, v127, v66
	v_add_f32_e32 v66, v96, v66
	v_add_f32_e32 v66, v97, v66
	v_cvt_pk_f16_f32 v154, v124, v125
	v_cvt_pk_f16_f32 v155, v126, v127
	ds_read_b64_tr_b16 v[112:113], v68 offset:2048
	ds_read_b64_tr_b16 v[114:115], v68 offset:2560
	s_waitcnt lgkmcnt(13)
	v_mfma_f32_32x32x16_f16 v[80:95], v[172:175], v[132:135], v[80:95]
	v_add_f32_e32 v66, v98, v66
	v_add_f32_e32 v66, v99, v66
	v_add_f32_e32 v66, v100, v66
	v_add_f32_e32 v66, v101, v66
	v_cvt_pk_f16_f32 v148, v96, v97
	v_cvt_pk_f16_f32 v149, v98, v99
	ds_read_b64_tr_b16 v[74:75], v68 offset:6144
	ds_read_b64_tr_b16 v[76:77], v68 offset:6656
	s_waitcnt lgkmcnt(14)
	v_mfma_f32_32x32x16_f16 v[48:63], v[168:171], v[132:135], v[48:63]
	v_add_f32_e32 v66, v102, v66
	v_add_f32_e32 v66, v103, v66
	v_add_f32_e32 v66, v104, v66
	v_add_f32_e32 v66, v105, v66
	v_cvt_pk_f16_f32 v150, v100, v101
	v_cvt_pk_f16_f32 v151, v102, v103
	ds_read_b64_tr_b16 v[70:71], v68 offset:3072
	ds_read_b64_tr_b16 v[72:73], v68 offset:3584
	s_waitcnt lgkmcnt(14)
	v_mfma_f32_32x32x16_f16 v[80:95], v[164:167], v[128:131], v[80:95]
	v_add_f32_e32 v66, v106, v66
	v_add_f32_e32 v66, v107, v66
	v_add_f32_e32 v66, v108, v66
	v_add_f32_e32 v79, v109, v66
	v_cvt_pk_f16_f32 v144, v104, v105
	v_cvt_pk_f16_f32 v145, v106, v107
	ds_read_b64_tr_b16 v[66:67], v68 offset:7168
	ds_read_b64_tr_b16 v[68:69], v68 offset:7680
	v_mfma_f32_32x32x16_f16 v[48:63], v[160:163], v[128:131], v[48:63]
	v_add_f32_e32 v79, v110, v79
	v_add_f32_e32 v79, v111, v79
	v_add_f32_e32 v79, 0, v79
	v_cvt_pk_f16_f32 v146, v108, v109
	v_cvt_pk_f16_f32 v147, v110, v111
.Lsqk_1b:
	s_add_i32 s33, s31, 2
	s_cmp_ge_u32 s33, s24
	s_cselect_b64 s[12:13], -1, 0
	s_and_b64 vcc, exec, s[12:13]
	s_cbranch_vccnz .LBB1_123
	s_add_i32 s2, s26, s22
	s_mov_b32 s3, m0
	s_mov_b32 m0, s2
	s_nop 0
	global_load_lds_dwordx4 v211, s[6:7]
	s_mov_b32 m0, s3

.LBB1_125:
	s_add_i32 s14, s14, 3
	s_cmp_lt_i32 s14, s50
	s_cbranch_scc1 .LBB1_127
	s_sub_i32 s51, s14, s50
	s_cmp_ge_i32 s51, 2
	s_cbranch_scc1 .Lsall_1b
	s_cmp_gt_i32 s14, s50
	s_cbranch_scc1 .Lmfill_1b
	v_subrev_u32_e32 v97, 27, v65
	v_subrev_u32_e32 v96, 59, v65
	v_cmp_le_u32_e32 vcc, v97, v207
	s_nop 1
	v_cndmask_b32_e32 v48, v252, v48, vcc
	v_cmp_lt_u32_e32 vcc, v96, v207
	s_nop 1
	v_cndmask_b32_e32 v81, v252, v81, vcc
	v_cmp_le_u32_e32 vcc, v96, v207
	v_subrev_u32_e32 v96, 26, v65
	s_nop 0
	v_cndmask_b32_e32 v80, v252, v80, vcc
	v_cmp_le_u32_e32 vcc, v96, v207
	v_subrev_u32_e32 v96, 57, v65
	s_nop 0
	v_cndmask_b32_e32 v49, v252, v49, vcc
	v_cmp_le_u32_e32 vcc, v96, v207
	v_subrev_u32_e32 v96, 25, v65
	s_nop 0
	v_cndmask_b32_e32 v82, v252, v82, vcc
	v_cmp_le_u32_e32 vcc, v96, v207
	v_subrev_u32_e32 v96, 56, v65
	s_nop 0
	v_cndmask_b32_e32 v50, v252, v50, vcc
	v_cmp_le_u32_e32 vcc, v96, v207
	v_subrev_u32_e32 v96, 24, v65
	s_nop 0
	v_cndmask_b32_e32 v83, v252, v83, vcc
	v_cmp_le_u32_e32 vcc, v96, v207
	v_subrev_u32_e32 v96, 51, v65
	s_nop 0
	v_cndmask_b32_e32 v51, v252, v51, vcc
	v_cmp_le_u32_e32 vcc, v96, v207
	v_subrev_u32_e32 v96, 19, v65
	s_nop 0
	v_cndmask_b32_e32 v84, v252, v84, vcc
	v_cmp_le_u32_e32 vcc, v96, v207
	v_subrev_u32_e32 v96, 50, v65
	s_nop 0
	v_cndmask_b32_e32 v52, v252, v52, vcc
	v_cmp_le_u32_e32 vcc, v96, v207
	v_subrev_u32_e32 v96, 18, v65
	s_nop 0
	v_cndmask_b32_e32 v85, v252, v85, vcc
	v_cmp_le_u32_e32 vcc, v96, v207
	v_subrev_u32_e32 v96, 49, v65
	s_nop 0
	v_cndmask_b32_e32 v53, v252, v53, vcc
	v_cmp_le_u32_e32 vcc, v96, v207
	v_subrev_u32_e32 v96, 17, v65
	s_nop 0
	v_cndmask_b32_e32 v86, v252, v86, vcc
	v_cmp_le_u32_e32 vcc, v96, v207
	v_subrev_u32_e32 v96, 48, v65
	s_nop 0
	v_cndmask_b32_e32 v54, v252, v54, vcc
	v_cmp_le_u32_e32 vcc, v96, v207
	v_add_u32_e32 v96, -16, v65
	s_nop 0
	v_cndmask_b32_e32 v87, v252, v87, vcc
	v_cmp_le_u32_e32 vcc, v96, v207
	v_subrev_u32_e32 v96, 43, v65
	s_nop 0
	v_cndmask_b32_e32 v55, v252, v55, vcc
	v_cmp_le_u32_e32 vcc, v96, v207
	v_add_u32_e32 v96, -11, v65
	s_nop 0
	v_cndmask_b32_e32 v88, v252, v88, vcc
	v_cmp_le_u32_e32 vcc, v96, v207
	v_subrev_u32_e32 v96, 42, v65
	s_nop 0
	v_cndmask_b32_e32 v56, v252, v56, vcc
	v_cmp_le_u32_e32 vcc, v96, v207
	v_add_u32_e32 v96, -10, v65
	s_nop 0
	v_cndmask_b32_e32 v89, v252, v89, vcc
	v_cmp_le_u32_e32 vcc, v96, v207
	v_subrev_u32_e32 v96, 41, v65
	s_nop 0
	v_cndmask_b32_e32 v57, v252, v57, vcc
	v_cmp_le_u32_e32 vcc, v96, v207
	v_add_u32_e32 v96, -9, v65
	s_nop 0
	v_cndmask_b32_e32 v90, v252, v90, vcc
	v_cmp_le_u32_e32 vcc, v96, v207
	v_subrev_u32_e32 v96, 40, v65
	s_nop 0
	v_cndmask_b32_e32 v58, v252, v58, vcc
	v_cmp_le_u32_e32 vcc, v96, v207
	v_add_u32_e32 v96, -8, v65
	s_nop 0
	v_cndmask_b32_e32 v91, v252, v91, vcc
	v_cmp_le_u32_e32 vcc, v96, v207
	v_subrev_u32_e32 v96, 35, v65
	s_nop 0
	v_cndmask_b32_e32 v59, v252, v59, vcc
	v_cmp_le_u32_e32 vcc, v96, v207
	v_add_u32_e32 v96, -3, v65
	s_nop 0
	v_cndmask_b32_e32 v92, v252, v92, vcc
	v_cmp_le_u32_e32 vcc, v96, v207
	v_subrev_u32_e32 v96, 34, v65
	s_nop 0
	v_cndmask_b32_e32 v60, v252, v60, vcc
	v_cmp_le_u32_e32 vcc, v96, v207
	v_add_u32_e32 v96, -2, v65
	s_nop 0
	v_cndmask_b32_e32 v93, v252, v93, vcc
	v_cmp_le_u32_e32 vcc, v96, v207
	v_subrev_u32_e32 v96, 33, v65
	s_nop 0
	v_cndmask_b32_e32 v61, v252, v61, vcc
	v_cmp_le_u32_e32 vcc, v96, v207
	v_add_u32_e32 v96, -1, v65
	s_nop 0
	v_cndmask_b32_e32 v94, v252, v94, vcc
	v_cmp_le_u32_e32 vcc, v96, v207
	v_subrev_u32_e32 v96, 32, v65
	s_nop 0
	v_cndmask_b32_e32 v62, v252, v62, vcc
	v_cmp_le_u32_e32 vcc, v96, v207
	s_nop 1
	v_cndmask_b32_e32 v95, v252, v95, vcc
	v_cmp_le_u32_e32 vcc, v65, v207
	s_nop 1
	v_cndmask_b32_e32 v63, v252, v63, vcc

.Lfqk_1b:
	v_add_u32_e32 v68, s25, v251
	ds_read_b64_tr_b16 v[200:201], v68
	ds_read_b64_tr_b16 v[202:203], v68 offset:512
	v_add_f32_e32 v48, v112, v113
	v_add_f32_e32 v48, v114, v48
	v_add_f32_e32 v48, v115, v48
	v_add_f32_e32 v48, v116, v48
	v_add_f32_e32 v48, v117, v48
	v_cvt_pk_f16_f32 v156, v112, v113
	v_cvt_pk_f16_f32 v157, v114, v115
	ds_read_b64_tr_b16 v[196:197], v68 offset:4096
	ds_read_b64_tr_b16 v[198:199], v68 offset:4608
	v_add_f32_e32 v48, v118, v48
	v_add_f32_e32 v48, v119, v48
	v_add_f32_e32 v48, v120, v48
	v_add_f32_e32 v66, v121, v48
	v_cvt_pk_f16_f32 v158, v116, v117
	v_cvt_pk_f16_f32 v159, v118, v119
	ds_read_b64_tr_b16 v[192:193], v68 offset:1024
	ds_read_b64_tr_b16 v[194:195], v68 offset:1536
	v_add_f32_e32 v66, v122, v66
	v_add_f32_e32 v66, v123, v66
	v_add_f32_e32 v66, v124, v66
	v_add_f32_e32 v66, v125, v66
	v_cvt_pk_f16_f32 v152, v120, v121
	v_cvt_pk_f16_f32 v153, v122, v123
	ds_read_b64_tr_b16 v[116:117], v68 offset:5120
	ds_read_b64_tr_b16 v[118:119], v68 offset:5632
	v_add_f32_e32 v66, v126, v66
	v_add_f32_e32 v66, v127, v66
	v_add_f32_e32 v66, v96, v66
	v_add_f32_e32 v66, v97, v66
	v_cvt_pk_f16_f32 v154, v124, v125
	v_cvt_pk_f16_f32 v155, v126, v127
	ds_read_b64_tr_b16 v[112:113], v68 offset:2048
	ds_read_b64_tr_b16 v[114:115], v68 offset:2560
	v_add_f32_e32 v66, v98, v66
	v_add_f32_e32 v66, v99, v66
	v_add_f32_e32 v66, v100, v66
	v_add_f32_e32 v66, v101, v66
	v_cvt_pk_f16_f32 v148, v96, v97
	v_cvt_pk_f16_f32 v149, v98, v99
	ds_read_b64_tr_b16 v[74:75], v68 offset:6144
	ds_read_b64_tr_b16 v[76:77], v68 offset:6656
	v_add_f32_e32 v66, v102, v66
	v_add_f32_e32 v66, v103, v66
	v_add_f32_e32 v66, v104, v66
	v_add_f32_e32 v66, v105, v66
	v_cvt_pk_f16_f32 v150, v100, v101
	v_cvt_pk_f16_f32 v151, v102, v103
	ds_read_b64_tr_b16 v[70:71], v68 offset:3072
	ds_read_b64_tr_b16 v[72:73], v68 offset:3584
	v_add_f32_e32 v66, v106, v66
	v_add_f32_e32 v66, v107, v66
	v_add_f32_e32 v66, v108, v66
	v_add_f32_e32 v79, v109, v66
	v_cvt_pk_f16_f32 v144, v104, v105
	v_cvt_pk_f16_f32 v145, v106, v107
	ds_read_b64_tr_b16 v[66:67], v68 offset:7168
	ds_read_b64_tr_b16 v[68:69], v68 offset:7680
	v_add_f32_e32 v79, v110, v79
	v_add_f32_e32 v79, v111, v79
	v_add_f32_e32 v79, 0, v79
	v_cvt_pk_f16_f32 v146, v108, v109
	v_cvt_pk_f16_f32 v147, v110, v111
	s_branch .Lsqk_1b
.Lfqk_0b:
	v_add_u32_e32 v206, s43, v209
	ds_read_b64_tr_b16 v[186:187], v206 offset:24576
	ds_read_b64_tr_b16 v[188:189], v206 offset:25088
	v_add_f32_e32 v50, v98, v99
	v_add_f32_e32 v50, v100, v50
	v_add_f32_e32 v50, v101, v50
	v_add_f32_e32 v50, v102, v50
	v_add_f32_e32 v50, v103, v50
	v_cvt_pk_f16_f32 v134, v98, v99
	v_cvt_pk_f16_f32 v135, v100, v101
	ds_read_b64_tr_b16 v[182:183], v206 offset:28672
	ds_read_b64_tr_b16 v[184:185], v206 offset:29184
	v_add_f32_e32 v50, v104, v50
	v_add_f32_e32 v50, v105, v50
	v_add_f32_e32 v50, v106, v50
	v_add_f32_e32 v98, v107, v50
	v_cvt_pk_f16_f32 v136, v102, v103
	v_cvt_pk_f16_f32 v137, v104, v105
	ds_read_b64_tr_b16 v[178:179], v206 offset:25600
	ds_read_b64_tr_b16 v[180:181], v206 offset:26112
	v_add_f32_e32 v98, v108, v98
	v_add_f32_e32 v98, v109, v98
	v_add_f32_e32 v98, v110, v98
	v_add_f32_e32 v98, v111, v98
	v_cvt_pk_f16_f32 v126, v106, v107
	v_cvt_pk_f16_f32 v127, v108, v109
	ds_read_b64_tr_b16 v[106:107], v206 offset:29696
	ds_read_b64_tr_b16 v[108:109], v206 offset:30208
	v_add_f32_e32 v98, v112, v98
	v_add_f32_e32 v98, v113, v98
	v_add_f32_e32 v98, v82, v98
	v_add_f32_e32 v98, v83, v98
	v_cvt_pk_f16_f32 v128, v110, v111
	v_cvt_pk_f16_f32 v129, v112, v113
	ds_read_b64_tr_b16 v[102:103], v206 offset:26624
	ds_read_b64_tr_b16 v[104:105], v206 offset:27136
	v_add_f32_e32 v98, v84, v98
	v_add_f32_e32 v98, v85, v98
	v_add_f32_e32 v98, v86, v98
	v_add_f32_e32 v110, v87, v98
	v_cvt_pk_f16_f32 v118, v82, v83
	v_cvt_pk_f16_f32 v119, v84, v85
	ds_read_b64_tr_b16 v[98:99], v206 offset:30720
	ds_read_b64_tr_b16 v[100:101], v206 offset:31232
	v_add_f32_e32 v82, v88, v110
	v_add_f32_e32 v82, v89, v82
	v_add_f32_e32 v82, v90, v82
	v_add_f32_e32 v82, v91, v82
	v_cvt_pk_f16_f32 v120, v86, v87
	v_cvt_pk_f16_f32 v121, v88, v89
	ds_read_b64_tr_b16 v[86:87], v206 offset:27648
	ds_read_b64_tr_b16 v[88:89], v206 offset:28160
	v_add_f32_e32 v82, v92, v82
	v_add_f32_e32 v82, v93, v82
	v_add_f32_e32 v82, v94, v82
	v_add_f32_e32 v110, v95, v82
	v_cvt_pk_f16_f32 v114, v90, v91
	v_cvt_pk_f16_f32 v115, v92, v93
	ds_read_b64_tr_b16 v[82:83], v206 offset:31744
	ds_read_b64_tr_b16 v[84:85], v206 offset:32256
	v_add_f32_e32 v90, v96, v110
	v_add_f32_e32 v90, v97, v90
	v_add_f32_e32 v90, 0, v90
	v_cvt_pk_f16_f32 v116, v94, v95
	v_cvt_pk_f16_f32 v117, v96, v97
	s_branch .Lsqk_0b
.Lsall_1b:
	s_mov_b64 s[14:15], 0
	s_branch .Lmpv_1b
.Lsall_0b:
	s_mov_b64 s[24:25], 0
	s_branch .Lmpv_0b
